# stack H plus: one static s_setprio 1 for waves 4-7 across the SB and MEM attention unit loops
# baseline (speedup 1.0000x reference)
.LBB0_785:
	s_mov_b32 s100, 0
	v_readfirstlane_b32 s0, v0
	s_lshr_b32 s0, s0, 8
	s_cmp_eq_u32 s0, 1
	s_cbranch_scc0 .Lsp2_skip
	s_setprio 1

.LBB0_836:
	s_setprio 0
	v_readlane_b32 s0, v254, 7
	v_readlane_b32 s1, v254, 8
	s_cmp_gt_i32 s1, 3
	v_readlane_b32 s2, v254, 9
	v_readlane_b32 s3, v254, 10
	s_cselect_b64 s[0:1], -1, 0
	s_and_b64 s[2:3], s[4:5], s[0:1]
	s_andn2_b64 vcc, exec, s[2:3]
	v_readlane_b32 s84, v254, 11
	s_cbranch_vccnz .LBB0_898
	v_cmp_gt_u32_e32 vcc, 32, v0
	s_waitcnt vmcnt(0)
	s_barrier
	s_and_saveexec_b64 s[4:5], vcc
	s_cbranch_execz .LBB0_845
	s_ashr_i32 s2, s90, 31
	v_mov_b32_e32 v2, s90
	v_mov_b32_e32 v3, s2
	v_readlane_b32 s2, v254, 2
	v_mov_b32_e32 v4, -1
	s_nop 0
	v_mad_i64_i32 v[2:3], s[2:3], s2, v0, v[2:3]
	s_mov_b64 s[2:3], 0x200
	s_nop 0
	v_cmp_gt_i64_e32 vcc, s[2:3], v[2:3]
	v_mov_b32_e32 v3, 0
	s_and_saveexec_b64 s[6:7], vcc
	s_cbranch_execz .LBB0_844
	v_ashrrev_i32_e32 v1, 31, v2
	v_lshrrev_b32_e32 v1, 29, v1
	v_add_u32_e32 v4, v2, v1
	v_and_b32_e32 v1, -8, v4
	v_sub_u32_e32 v3, v2, v1
	v_cmp_lt_i32_e32 vcc, -1, v3
	s_and_saveexec_b64 s[2:3], vcc
	s_xor_b64 s[8:9], exec, s[2:3]
	v_lshlrev_b32_e32 v2, 6, v3
	s_or_saveexec_b64 s[8:9], s[8:9]
	v_ashrrev_i32_e32 v4, 3, v4
	s_xor_b64 exec, exec, s[8:9]
	v_lshl_add_u32 v2, v3, 6, v3
	s_or_b64 exec, exec, s[8:9]
	v_add_u32_e32 v1, v2, v4
	v_ashrrev_i32_e32 v2, 31, v1
	v_lshrrev_b32_e32 v2, 26, v2
	v_add_u32_e32 v2, v1, v2
	v_ashrrev_i32_e32 v3, 6, v2
	v_lshlrev_b32_e32 v4, 3, v3
	v_sub_u32_e32 v3, 64, v4
	v_min_i32_e32 v5, 8, v3
	v_sub_u32_e32 v3, 0, v5
	v_max_i32_e32 v3, v5, v3
	v_cvt_f32_u32_e32 v6, v3
	v_and_b32_e32 v2, 0xffffffc0, v2
	v_sub_u32_e32 v8, 0, v3
	v_sub_u32_e32 v1, v1, v2
	v_rcp_iflag_f32_e32 v6, v6
	v_sub_u32_e32 v2, 0, v1
	v_max_i32_e32 v2, v1, v2
	v_xor_b32_e32 v7, v1, v5
	v_mul_f32_e32 v6, 0x4f7ffffe, v6
	v_cvt_u32_f32_e32 v6, v6
	v_ashrrev_i32_e32 v7, 31, v7
	v_mul_lo_u32 v8, v8, v6
	v_mul_hi_u32 v8, v6, v8
	v_add_u32_e32 v6, v6, v8
	v_mul_hi_u32 v6, v2, v6
	v_mul_lo_u32 v8, v6, v3
	v_sub_u32_e32 v2, v2, v8
	v_add_u32_e32 v9, 1, v6
	v_cmp_ge_u32_e32 vcc, v2, v3
	v_sub_u32_e32 v8, v2, v3
	s_nop 0
	v_cndmask_b32_e32 v6, v6, v9, vcc
	v_cndmask_b32_e32 v2, v2, v8, vcc
	v_add_u32_e32 v8, 1, v6
	v_cmp_ge_u32_e32 vcc, v2, v3
	s_nop 1
	v_cndmask_b32_e32 v2, v6, v8, vcc
	v_xor_b32_e32 v2, v2, v7
	v_sub_u32_e32 v3, v2, v7
	v_mul_lo_u32 v2, v3, v5
	v_sub_u32_e32 v1, v1, v2
	v_add_u32_e32 v4, v4, v1
